# gu K-loop: half of each SP2 LDS-DMA burst issued between the MFMAs of the same sub-phase instead of in the load block (vmcnt counts re-derived)
# baseline (speedup 1.0000x reference)
.LBB0_1642:
	s_add_u32 s4, s24, 0x80
	s_waitcnt lgkmcnt(0)
	s_addc_u32 s5, s25, 0
	s_add_u32 s24, s22, 0x80
	s_addc_u32 s25, s23, 0
	s_barrier
	s_setprio 1
	s_waitcnt lgkmcnt(6)
	v_mfma_f32_16x16x128_f8f6f4 v[190:193], v[26:33], v[58:65], v[190:193]
	v_mfma_f32_16x16x128_f8f6f4 v[186:189], v[18:25], v[58:65], v[186:189]
	s_waitcnt lgkmcnt(4)
	v_mfma_f32_16x16x128_f8f6f4 v[174:177], v[26:33], v[50:57], v[174:177]
	v_mfma_f32_16x16x128_f8f6f4 v[170:173], v[18:25], v[50:57], v[170:173]
	s_waitcnt lgkmcnt(2)
	v_mfma_f32_16x16x128_f8f6f4 v[158:161], v[26:33], v[42:49], v[158:161]
	v_mfma_f32_16x16x128_f8f6f4 v[154:157], v[18:25], v[42:49], v[154:157]
	s_waitcnt lgkmcnt(0)
	v_mfma_f32_16x16x128_f8f6f4 v[142:145], v[26:33], v[34:41], v[142:145]
	v_mfma_f32_16x16x128_f8f6f4 v[138:141], v[18:25], v[34:41], v[138:141]
	s_setprio 0
	s_setprio 1
	v_mfma_f32_16x16x128_f8f6f4 v[182:185], v[10:17], v[58:65], v[182:185]
	v_mfma_f32_16x16x128_f8f6f4 v[178:181], v[2:9], v[58:65], v[178:181]
	v_mfma_f32_16x16x128_f8f6f4 v[166:169], v[10:17], v[50:57], v[166:169]
	v_mfma_f32_16x16x128_f8f6f4 v[162:165], v[2:9], v[50:57], v[162:165]
	v_mfma_f32_16x16x128_f8f6f4 v[150:153], v[10:17], v[42:49], v[150:153]
	v_mfma_f32_16x16x128_f8f6f4 v[146:149], v[2:9], v[42:49], v[146:149]
	v_mfma_f32_16x16x128_f8f6f4 v[134:137], v[10:17], v[34:41], v[134:137]
	v_mfma_f32_16x16x128_f8f6f4 v[130:133], v[2:9], v[34:41], v[130:133]
	s_setprio 0
	s_barrier
	ds_read_b128 v[34:37], v218 offset:49152
	ds_read_b128 v[38:41], v218 offset:50176
	ds_read_b128 v[42:45], v218 offset:51200
	ds_read_b128 v[46:49], v218 offset:52224
	ds_read_b128 v[50:53], v218 offset:53248
	ds_read_b128 v[54:57], v218 offset:54272
	ds_read_b128 v[58:61], v218 offset:55296
	ds_read_b128 v[62:65], v218 offset:56320
	s_mov_b32 m0, s40
	s_nop 0
	global_load_lds_dwordx4 v210, s[24:25]
	s_add_u32 s22, s22, 0x20080
	s_mov_b32 m0, s41
	s_nop 0
	global_load_lds_dwordx4 v212, s[24:25]
	s_addc_u32 s23, s23, 0
	s_mov_b32 m0, s44
	s_nop 0
	global_load_lds_dwordx4 v210, s[22:23]
	s_nop 0
	s_nop 0
	s_waitcnt vmcnt(5)
	s_waitcnt lgkmcnt(0)
	s_barrier
	s_setprio 1
	s_waitcnt lgkmcnt(6)
	v_mfma_f32_16x16x128_f8f6f4 v[126:129], v[26:33], v[34:41], v[126:129]
	v_mfma_f32_16x16x128_f8f6f4 v[122:125], v[18:25], v[34:41], v[122:125]
	s_mov_b32 m0, s45
	s_nop 0
	global_load_lds_dwordx4 v212, s[22:23]
	s_waitcnt lgkmcnt(4)
	v_mfma_f32_16x16x128_f8f6f4 v[110:113], v[26:33], v[42:49], v[110:113]
	v_mfma_f32_16x16x128_f8f6f4 v[106:109], v[18:25], v[42:49], v[106:109]
	s_waitcnt lgkmcnt(2)
	v_mfma_f32_16x16x128_f8f6f4 v[86:89], v[26:33], v[50:57], v[86:89]
	v_mfma_f32_16x16x128_f8f6f4 v[82:85], v[18:25], v[50:57], v[82:85]
	s_mov_b32 m0, s42
	s_nop 0
	global_load_lds_dwordx4 v194, s[4:5]
	s_waitcnt lgkmcnt(0)
	v_mfma_f32_16x16x128_f8f6f4 v[70:73], v[26:33], v[58:65], v[70:73]
	v_mfma_f32_16x16x128_f8f6f4 v[66:69], v[18:25], v[58:65], v[66:69]
	s_setprio 0
	s_setprio 1
	v_mfma_f32_16x16x128_f8f6f4 v[118:121], v[10:17], v[34:41], v[118:121]
	v_mfma_f32_16x16x128_f8f6f4 v[114:117], v[2:9], v[34:41], v[114:117]
	s_mov_b32 m0, s43
	s_nop 0
	global_load_lds_dwordx4 v227, s[4:5]
	v_mfma_f32_16x16x128_f8f6f4 v[102:105], v[10:17], v[42:49], v[102:105]
	v_mfma_f32_16x16x128_f8f6f4 v[90:93], v[2:9], v[42:49], v[90:93]
	v_mfma_f32_16x16x128_f8f6f4 v[98:101], v[10:17], v[50:57], v[98:101]
	v_mfma_f32_16x16x128_f8f6f4 v[94:97], v[2:9], v[50:57], v[94:97]
	v_mfma_f32_16x16x128_f8f6f4 v[78:81], v[10:17], v[58:65], v[78:81]
	v_mfma_f32_16x16x128_f8f6f4 v[74:77], v[2:9], v[58:65], v[74:77]
	s_setprio 0
	s_barrier
	s_add_i32 s55, s55, 2
	s_add_u32 s20, s20, 0x100
	s_addc_u32 s21, s21, 0
	s_cmp_gt_u32 s55, 5
	s_cbranch_scc1 .LBB0_1655

.LBB0_1647:
	s_xor_b64 s[26:27], s[4:5], -1
	s_add_u32 s24, s24, 0x100
	s_addc_u32 s25, s25, 0
	s_add_u32 s28, s15, s20
	s_addc_u32 s29, s54, s21
	s_cmpk_eq_i32 s20, 0x300
	s_cselect_b64 s[4:5], -1, 0
	s_waitcnt lgkmcnt(0)
	s_and_b64 s[22:23], s[4:5], exec
	v_cndmask_b32_e64 v194, v226, v220, s[4:5]
	s_cselect_b32 s25, s3, s25
	s_cselect_b32 s24, s2, s24
	v_cndmask_b32_e64 v227, v223, v219, s[4:5]
	s_cselect_b32 s23, s17, s29
	s_cselect_b32 s22, s16, s28
	s_barrier
	s_setprio 1
	s_waitcnt lgkmcnt(6)
	v_mfma_f32_16x16x128_f8f6f4 v[190:193], v[26:33], v[58:65], v[190:193]
	v_mfma_f32_16x16x128_f8f6f4 v[186:189], v[18:25], v[58:65], v[186:189]
	s_waitcnt lgkmcnt(4)
	v_mfma_f32_16x16x128_f8f6f4 v[174:177], v[26:33], v[50:57], v[174:177]
	v_mfma_f32_16x16x128_f8f6f4 v[170:173], v[18:25], v[50:57], v[170:173]
	s_waitcnt lgkmcnt(2)
	v_mfma_f32_16x16x128_f8f6f4 v[158:161], v[26:33], v[42:49], v[158:161]
	v_mfma_f32_16x16x128_f8f6f4 v[154:157], v[18:25], v[42:49], v[154:157]
	s_waitcnt lgkmcnt(0)
	v_mfma_f32_16x16x128_f8f6f4 v[142:145], v[26:33], v[34:41], v[142:145]
	v_mfma_f32_16x16x128_f8f6f4 v[138:141], v[18:25], v[34:41], v[138:141]
	s_setprio 0
	s_setprio 1
	v_mfma_f32_16x16x128_f8f6f4 v[182:185], v[10:17], v[58:65], v[182:185]
	v_mfma_f32_16x16x128_f8f6f4 v[178:181], v[2:9], v[58:65], v[178:181]
	v_mfma_f32_16x16x128_f8f6f4 v[166:169], v[10:17], v[50:57], v[166:169]
	v_mfma_f32_16x16x128_f8f6f4 v[162:165], v[2:9], v[50:57], v[162:165]
	v_mfma_f32_16x16x128_f8f6f4 v[150:153], v[10:17], v[42:49], v[150:153]
	v_mfma_f32_16x16x128_f8f6f4 v[146:149], v[2:9], v[42:49], v[146:149]
	v_mfma_f32_16x16x128_f8f6f4 v[134:137], v[10:17], v[34:41], v[134:137]
	v_mfma_f32_16x16x128_f8f6f4 v[130:133], v[2:9], v[34:41], v[130:133]
	s_setprio 0
	s_barrier
	ds_read_b128 v[58:61], v218 offset:16384
	ds_read_b128 v[62:65], v218 offset:17408
	ds_read_b128 v[50:53], v218 offset:18432
	ds_read_b128 v[54:57], v218 offset:19456
	ds_read_b128 v[42:45], v218 offset:20480
	ds_read_b128 v[46:49], v218 offset:21504
	ds_read_b128 v[34:37], v218 offset:22528
	ds_read_b128 v[38:41], v218 offset:23552
	s_mov_b32 m0, s31
	s_nop 0
	global_load_lds_dwordx4 v210, s[22:23]
	s_nop 0
	s_mov_b32 m0, s34
	s_nop 0
	global_load_lds_dwordx4 v212, s[22:23]
	s_add_u32 s28, s22, 0x20000
	s_addc_u32 s29, s23, 0
	s_mov_b32 m0, s35
	s_nop 0
	global_load_lds_dwordx4 v210, s[28:29]
	s_and_b64 vcc, exec, s[26:27]
	s_mov_b32 m0, s36
	s_nop 0
	global_load_lds_dwordx4 v212, s[28:29]
	s_nop 0
	s_mov_b64 s[28:29], -1
	s_cbranch_vccz .LBB0_1649
	s_waitcnt vmcnt(6)
	s_mov_b64 s[28:29], 0
.LBB0_1649:
	s_andn2_b64 vcc, exec, s[28:29]
	s_cbranch_vccnz .LBB0_1651
	s_waitcnt vmcnt(10)
.LBB0_1651:
	s_waitcnt lgkmcnt(0)
	v_cndmask_b32_e64 v228, v224, v221, s[4:5]
	v_cndmask_b32_e64 v229, v225, v222, s[4:5]
	s_barrier
	s_setprio 1
	s_waitcnt lgkmcnt(6)
	v_mfma_f32_16x16x128_f8f6f4 v[126:129], v[26:33], v[58:65], v[126:129]
	v_mfma_f32_16x16x128_f8f6f4 v[122:125], v[18:25], v[58:65], v[122:125]
	s_waitcnt lgkmcnt(4)
	v_mfma_f32_16x16x128_f8f6f4 v[110:113], v[26:33], v[50:57], v[110:113]
	v_mfma_f32_16x16x128_f8f6f4 v[106:109], v[18:25], v[50:57], v[106:109]
	s_mov_b32 m0, s30
	s_nop 0
	global_load_lds_dwordx4 v194, s[24:25]
	s_waitcnt lgkmcnt(2)
	v_mfma_f32_16x16x128_f8f6f4 v[86:89], v[26:33], v[42:49], v[86:89]
	v_mfma_f32_16x16x128_f8f6f4 v[82:85], v[18:25], v[42:49], v[82:85]
	s_waitcnt lgkmcnt(0)
	v_mfma_f32_16x16x128_f8f6f4 v[70:73], v[26:33], v[34:41], v[70:73]
	v_mfma_f32_16x16x128_f8f6f4 v[66:69], v[18:25], v[34:41], v[66:69]
	s_setprio 0
	s_setprio 1
	v_mfma_f32_16x16x128_f8f6f4 v[118:121], v[10:17], v[58:65], v[118:121]
	v_mfma_f32_16x16x128_f8f6f4 v[114:117], v[2:9], v[58:65], v[114:117]
	s_mov_b32 m0, s37
	s_nop 0
	global_load_lds_dwordx4 v227, s[24:25]
	v_mfma_f32_16x16x128_f8f6f4 v[102:105], v[10:17], v[50:57], v[102:105]
	v_mfma_f32_16x16x128_f8f6f4 v[90:93], v[2:9], v[50:57], v[90:93]
	v_mfma_f32_16x16x128_f8f6f4 v[98:101], v[10:17], v[42:49], v[98:101]
	v_mfma_f32_16x16x128_f8f6f4 v[94:97], v[2:9], v[42:49], v[94:97]
	v_mfma_f32_16x16x128_f8f6f4 v[78:81], v[10:17], v[34:41], v[78:81]
	v_mfma_f32_16x16x128_f8f6f4 v[74:77], v[2:9], v[34:41], v[74:77]
	s_setprio 0
	s_barrier
	v_add_u32_e32 v2, 0x18000, v217
	v_add_u32_e32 v6, 0x1c000, v217
	ds_read_b128 v[26:29], v2
	ds_read_b128 v[30:33], v2 offset:1024
	ds_read_b128 v[18:21], v2 offset:2048
	ds_read_b128 v[22:25], v2 offset:3072
	ds_read_b128 v[10:13], v6
	ds_read_b128 v[14:17], v6 offset:1024
	ds_read_b128 v[2:5], v6 offset:2048
	ds_read_b128 v[6:9], v6 offset:3072
	ds_read_b128 v[58:61], v218 offset:32768
	ds_read_b128 v[62:65], v218 offset:33792
	ds_read_b128 v[50:53], v218 offset:34816
	ds_read_b128 v[54:57], v218 offset:35840
	ds_read_b128 v[42:45], v218 offset:36864
	ds_read_b128 v[46:49], v218 offset:37888
	ds_read_b128 v[34:37], v218 offset:38912
	ds_read_b128 v[38:41], v218 offset:39936
	s_mov_b32 m0, s38
	s_nop 0
	global_load_lds_dwordx4 v228, s[24:25]
	s_and_b64 vcc, exec, s[26:27]
	s_mov_b32 m0, s39
	s_nop 0
	global_load_lds_dwordx4 v229, s[24:25]
	s_mov_b64 s[4:5], -1
	s_cbranch_vccz .LBB0_1653
	s_waitcnt vmcnt(8)
	s_mov_b64 s[4:5], 0
